# speedup vs baseline: 1.0119x; 1.0060x over previous
_Z6k_gramILi0EEvPK15HIP_vector_typeIjLj4EEPyPf:
	s_load_dwordx4 s[8:11], s[0:1], 0x0
	s_load_dwordx2 s[4:5], s[0:1], 0x10
	s_lshl_b32 s0, s2, 2
	s_and_b32 s0, s0, 28
	s_ashr_i32 s1, s2, 6
	s_add_i32 s16, s0, s1
	v_readfirstlane_b32 s23, v0
	s_ashr_i32 s17, s16, 31
	s_lshr_b32 s21, s23, 6
	s_bfe_u32 s18, s23, 0x20006
	s_lshr_b32 s22, s2, 3
	s_bfe_u32 s20, s2, 0x30003
	s_lshl_b64 s[0:1], s[16:17], 20
	s_waitcnt lgkmcnt(0)
	s_add_u32 s12, s8, s0
	v_mov_b32_e32 v1, 0x20000
	s_addc_u32 s0, s9, s1
	s_lshl_b32 s1, s20, 2
	v_lshl_or_b32 v1, v0, 2, v1
	v_bfrev_b32_e32 v2, 1
	s_cmp_lt_u32 s20, 4
	ds_write_b32 v1, v2
	s_cselect_b32 s24, 5, 4
	s_mov_b32 s15, 0x20000
	s_and_b32 s13, s0, 0xffff
	s_mov_b32 s14, 0x100000
	v_lshlrev_b32_e32 v166, 4, v0
	s_lshl_b32 s25, s21, 10
	s_lshl_b32 s0, s20, 17
	s_mov_b32 m0, s25
	s_nop 0
	buffer_load_dwordx4 v166, s[12:15], s0 offen lds
	s_add_i32 s26, s25, 0x2000
	s_or_b32 s2, s0, 0x2000
	s_mov_b32 m0, s26
	s_nop 0
	buffer_load_dwordx4 v166, s[12:15], s2 offen lds
	s_add_i32 s27, s25, 0x4000
	s_or_b32 s2, s0, 0x8000
	s_mov_b32 m0, s27
	s_nop 0
	buffer_load_dwordx4 v166, s[12:15], s2 offen lds
	s_add_i32 s28, s25, 0x6000
	s_or_b32 s2, s0, 0xa000
	s_mov_b32 m0, s28
	s_nop 0
	buffer_load_dwordx4 v166, s[12:15], s2 offen lds
	s_add_i32 s34, s25, 0x10000
	s_or_b32 s2, s0, 0x10000
	s_mov_b32 m0, s34
	s_nop 0
	buffer_load_dwordx4 v166, s[12:15], s2 offen lds
	s_add_i32 s35, s25, 0x12000
	s_or_b32 s2, s0, 0x12000
	s_mov_b32 m0, s35
	s_nop 0
	buffer_load_dwordx4 v166, s[12:15], s2 offen lds
	s_add_i32 s36, s25, 0x14000
	s_or_b32 s2, s0, 0x18000
	s_mov_b32 m0, s36
	s_nop 0
	buffer_load_dwordx4 v166, s[12:15], s2 offen lds
	s_add_i32 s37, s25, 0x16000
	s_or_b32 s2, s0, 0x1a000
	s_mov_b32 m0, s37
	s_nop 0
	buffer_load_dwordx4 v166, s[12:15], s2 offen lds
	s_add_i32 s29, s25, 0x8000
	s_or_b32 s2, s0, 0x4000
	s_mov_b32 m0, s29
	s_nop 0
	buffer_load_dwordx4 v166, s[12:15], s2 offen lds
	s_add_i32 s30, s25, 0xa000
	s_or_b32 s2, s0, 0x6000
	s_mov_b32 m0, s30
	s_nop 0
	buffer_load_dwordx4 v166, s[12:15], s2 offen lds
	s_add_i32 s31, s25, 0xc000
	s_or_b32 s2, s0, 0xc000
	s_mov_b32 m0, s31
	s_nop 0
	buffer_load_dwordx4 v166, s[12:15], s2 offen lds
	s_add_i32 s33, s25, 0xe000
	s_or_b32 s2, s0, 0xe000
	s_mov_b32 m0, s33
	s_nop 0
	buffer_load_dwordx4 v166, s[12:15], s2 offen lds
	s_add_i32 s38, s25, 0x18000
	s_or_b32 s2, s0, 0x14000
	s_mov_b32 m0, s38
	s_nop 0
	buffer_load_dwordx4 v166, s[12:15], s2 offen lds
	s_add_i32 s39, s25, 0x1a000
	s_or_b32 s2, s0, 0x16000
	s_mov_b32 m0, s39
	s_nop 0
	buffer_load_dwordx4 v166, s[12:15], s2 offen lds
	s_add_i32 s40, s25, 0x1c000
	s_or_b32 s2, s0, 0x1c000
	s_mov_b32 m0, s40
	s_nop 0
	buffer_load_dwordx4 v166, s[12:15], s2 offen lds
	s_add_i32 s42, s25, 0x1e000
	s_or_b32 s2, s0, 0x1e000
	s_mov_b32 m0, s42
	s_nop 0
	buffer_load_dwordx4 v166, s[12:15], s2 offen lds
	s_lshl_b32 s0, s23, 9
	s_lshl_b32 s2, s23, 8
	v_and_b32_e32 v167, 15, v0
	v_bfe_u32 v160, v0, 4, 2
	s_and_b32 s0, s0, 0x10000
	s_and_b32 s2, s2, 0x4000
	v_lshlrev_b32_e32 v128, 9, v160
	v_lshlrev_b32_e32 v129, 4, v167
	s_or_b32 s0, s0, s2
	v_or3_b32 v124, s0, v128, v129
	s_waitcnt vmcnt(8)
	s_waitcnt lgkmcnt(0)
	s_barrier
	ds_read_b128 v[0:3], v124
	ds_read_b128 v[4:7], v124 offset:256
	ds_read_b128 v[8:11], v124 offset:2048
	ds_read_b128 v[12:15], v124 offset:2304
	ds_read_b128 v[16:19], v124 offset:4096
	ds_read_b128 v[20:23], v124 offset:4352
	ds_read_b128 v[24:27], v124 offset:6144
	ds_read_b128 v[28:31], v124 offset:6400
	ds_read_b128 v[32:35], v124 offset:8192
	ds_read_b128 v[36:39], v124 offset:8448
	ds_read_b128 v[40:43], v124 offset:10240
	ds_read_b128 v[44:47], v124 offset:10496
	ds_read_b128 v[48:51], v124 offset:12288
	ds_read_b128 v[52:55], v124 offset:12544
	ds_read_b128 v[56:59], v124 offset:14336
	ds_read_b128 v[60:63], v124 offset:14592
	s_lshr_b32 s41, s23, 8
	s_lshl_b32 s0, s41, 14
	s_lshl_b32 s50, s24, 2
	v_or3_b32 v168, s0, v128, v129
	s_or_b32 s43, s18, s1
	s_lshl_b32 s0, s16, 10
	s_lshl_b32 s1, s43, 5
	ds_read_b128 v[128:131], v168
	ds_read_b128 v[132:135], v168 offset:256
	ds_read_b128 v[136:139], v168 offset:2048
	ds_read_b128 v[140:143], v168 offset:2304
	s_or_b32 s0, s1, s0
	v_or_b32_e32 v144, s0, v167
	v_lshlrev_b32_e32 v146, 2, v160
	v_ashrrev_i32_e32 v145, 31, v144
	v_lshl_add_u64 v[164:165], v[144:145], 2, s[4:5]
	v_or_b32_e32 v144, 1, v146
	v_cmp_eq_u32_e64 s[2:3], v144, v167
	v_or_b32_e32 v144, 2, v146
	s_waitcnt vmcnt(8)
	v_cmp_eq_u32_e64 s[4:5], v144, v167
	v_or_b32_e32 v144, 3, v146
	s_add_i32 s44, s50, -1
	s_lshl_b32 s45, s22, 2
	v_cmp_eq_u32_e64 s[0:1], v146, v167
	v_cmp_eq_u32_e64 s[6:7], v144, v167
	v_add_u32_e32 v169, 0x10000, v168
	v_add_u32_e32 v170, 0x10100, v168
	v_add_u32_e32 v171, 0x10800, v168
	v_add_u32_e32 v172, 0x10900, v168
	s_barrier
	s_add_i32 s8, s45, 28
	s_and_b32 s8, s8, 28
	s_add_i32 s8, s41, s8
	s_lshl_b32 s8, s8, 1
	s_add_i32 s9, s8, 4
	s_add_i32 s8, s8, 5
	v_mov_b32_e32 v148, s9
	v_mov_b32_e32 v149, s8
	ds_read_b128 v[148:151], v168 offset:4096
	s_waitcnt lgkmcnt(4)
	v_mfma_f32_16x16x32_bf16 v[144:147], v[0:3], v[128:131], 0
	v_mfma_f32_16x16x32_bf16 v[128:131], v[4:7], v[128:131], 0
	ds_read_b128 v[156:159], v168 offset:4352
	s_waitcnt lgkmcnt(4)
	v_mfma_f32_16x16x32_bf16 v[152:155], v[0:3], v[132:135], 0
	v_mfma_f32_16x16x32_bf16 v[132:135], v[4:7], v[132:135], 0
	s_waitcnt lgkmcnt(3)
	v_mfma_f32_16x16x32_bf16 v[144:147], v[8:11], v[136:139], v[144:147]
	ds_read_b128 v[174:177], v168 offset:6144
	v_mfma_f32_16x16x32_bf16 v[128:131], v[12:15], v[136:139], v[128:131]
	s_waitcnt lgkmcnt(3)
	v_mfma_f32_16x16x32_bf16 v[136:139], v[8:11], v[140:143], v[152:155]
	s_nop 2
	ds_read_b128 v[152:155], v168 offset:6400
	v_mfma_f32_16x16x32_bf16 v[132:135], v[12:15], v[140:143], v[132:135]
	s_waitcnt lgkmcnt(3)
	v_mfma_f32_16x16x32_bf16 v[140:143], v[16:19], v[148:151], v[144:147]
	s_nop 2
	ds_read_b128 v[144:147], v168 offset:8192
	v_mfma_f32_16x16x32_bf16 v[128:131], v[20:23], v[148:151], v[128:131]
	ds_read_b128 v[148:151], v168 offset:8448
	s_waitcnt lgkmcnt(4)
	v_mfma_f32_16x16x32_bf16 v[136:139], v[16:19], v[156:159], v[136:139]
	v_mfma_f32_16x16x32_bf16 v[132:135], v[20:23], v[156:159], v[132:135]
	ds_read_b128 v[156:159], v168 offset:10240
	s_waitcnt lgkmcnt(4)
	v_mfma_f32_16x16x32_bf16 v[140:143], v[24:27], v[174:177], v[140:143]
	v_mfma_f32_16x16x32_bf16 v[128:131], v[28:31], v[174:177], v[128:131]
	s_waitcnt lgkmcnt(3)
	v_mfma_f32_16x16x32_bf16 v[136:139], v[24:27], v[152:155], v[136:139]
	ds_read_b128 v[174:177], v168 offset:10496
	v_mfma_f32_16x16x32_bf16 v[132:135], v[28:31], v[152:155], v[132:135]
	ds_read_b128 v[152:155], v168 offset:12288
	s_waitcnt lgkmcnt(4)
	v_mfma_f32_16x16x32_bf16 v[140:143], v[32:35], v[144:147], v[140:143]
	v_mfma_f32_16x16x32_bf16 v[128:131], v[36:39], v[144:147], v[128:131]
	ds_read_b128 v[144:147], v168 offset:12544
	s_waitcnt lgkmcnt(4)
	v_mfma_f32_16x16x32_bf16 v[136:139], v[32:35], v[148:151], v[136:139]
	v_mfma_f32_16x16x32_bf16 v[132:135], v[36:39], v[148:151], v[132:135]
	ds_read_b128 v[148:151], v168 offset:14336
	s_waitcnt lgkmcnt(4)
	v_mfma_f32_16x16x32_bf16 v[140:143], v[40:43], v[156:159], v[140:143]
	v_mfma_f32_16x16x32_bf16 v[128:131], v[44:47], v[156:159], v[128:131]
	ds_read_b128 v[156:159], v168 offset:14592
	s_waitcnt lgkmcnt(4)
	v_mfma_f32_16x16x32_bf16 v[136:139], v[40:43], v[174:177], v[136:139]
	v_mfma_f32_16x16x32_bf16 v[132:135], v[44:47], v[174:177], v[132:135]
	s_waitcnt lgkmcnt(3)
	v_mfma_f32_16x16x32_bf16 v[140:143], v[48:51], v[152:155], v[140:143]
	ds_read_b128 v[174:177], v168 offset:32768
	v_mfma_f32_16x16x32_bf16 v[128:131], v[52:55], v[152:155], v[128:131]
	ds_read_b128 v[152:155], v168 offset:33024
	s_waitcnt lgkmcnt(4)
	v_mfma_f32_16x16x32_bf16 v[136:139], v[48:51], v[144:147], v[136:139]
	v_mfma_f32_16x16x32_bf16 v[132:135], v[52:55], v[144:147], v[132:135]
	ds_read_b128 v[144:147], v168 offset:34816
	s_waitcnt lgkmcnt(4)
	v_mfma_f32_16x16x32_bf16 v[140:143], v[56:59], v[148:151], v[140:143]
	v_mfma_f32_16x16x32_bf16 v[128:131], v[60:63], v[148:151], v[128:131]
	ds_read_b128 v[148:151], v168 offset:35072
	s_waitcnt lgkmcnt(4)
	v_mfma_f32_16x16x32_bf16 v[136:139], v[56:59], v[156:159], v[136:139]
	v_mfma_f32_16x16x32_bf16 v[132:135], v[60:63], v[156:159], v[132:135]
	s_waitcnt vmcnt(0)
	s_barrier
	ds_read_b128 v[64:67], v124 offset:32768
	ds_read_b128 v[68:71], v124 offset:33024
	ds_read_b128 v[72:75], v124 offset:34816
	ds_read_b128 v[76:79], v124 offset:35072
	ds_read_b128 v[80:83], v124 offset:36864
	ds_read_b128 v[84:87], v124 offset:37120
	ds_read_b128 v[88:91], v124 offset:38912
	ds_read_b128 v[92:95], v124 offset:39168
	ds_read_b128 v[96:99], v124 offset:40960
	ds_read_b128 v[100:103], v124 offset:41216
	ds_read_b128 v[104:107], v124 offset:43008
	ds_read_b128 v[108:111], v124 offset:43264
	ds_read_b128 v[112:115], v124 offset:45056
	ds_read_b128 v[116:119], v124 offset:45312
	ds_read_b128 v[120:123], v124 offset:47104
	ds_read_b128 v[124:127], v124 offset:47360
	ds_read_b128 v[174:177], v168 offset:32768
	ds_read_b128 v[152:155], v168 offset:33024
	ds_read_b128 v[144:147], v168 offset:34816
	ds_read_b128 v[148:151], v168 offset:35072
	s_waitcnt lgkmcnt(0)
	s_and_b32 s8, s45, 28
	s_add_i32 s8, s8, s41
	s_lshl_b32 s19, s8, 1
	s_or_b32 s51, s19, 1
	v_mov_b32_e32 v156, s51
	v_mov_b32_e32 v157, s19
	ds_read_b128 v[156:159], v168 offset:36864
	s_waitcnt lgkmcnt(4)
	v_mfma_f32_16x16x32_bf16 v[140:143], v[64:67], v[174:177], v[140:143]
	s_min_u32 s9, s44, 4
	s_add_i32 s46, s9, s45
	v_mov_b32_e32 v202, s19
	v_mfma_f32_16x16x32_bf16 v[128:131], v[68:71], v[174:177], v[128:131]
	v_mov_b32_e32 v206, s51
	s_and_b32 s46, s46, 28
	s_and_b32 s47, s9, 2
	s_lshl_b32 s9, s9, 14
	s_or_b32 s46, s47, s46
	s_and_b32 s9, s9, 0x4000
	ds_read_b128 v[174:177], v168 offset:37120
	s_waitcnt lgkmcnt(4)
	v_mfma_f32_16x16x32_bf16 v[136:139], v[64:67], v[152:155], v[136:139]
	s_lshl_b32 s46, s46, 15
	s_or_b32 s9, s46, s9
	s_mov_b32 m0, s25
	s_nop 0
	buffer_load_dwordx4 v166, s[12:15], s9 offen lds
	v_mfma_f32_16x16x32_bf16 v[132:135], v[68:71], v[152:155], v[132:135]
	ds_read_b128 v[152:155], v168 offset:38912
	s_waitcnt lgkmcnt(4)
	v_mfma_f32_16x16x32_bf16 v[140:143], v[72:75], v[144:147], v[140:143]
	v_mfma_f32_16x16x32_bf16 v[128:131], v[76:79], v[144:147], v[128:131]
	ds_read_b128 v[144:147], v168 offset:39168
	s_waitcnt lgkmcnt(4)
	v_mfma_f32_16x16x32_bf16 v[136:139], v[72:75], v[148:151], v[136:139]
	v_mfma_f32_16x16x32_bf16 v[132:135], v[76:79], v[148:151], v[132:135]
	ds_read_b128 v[148:151], v168 offset:40960
	s_waitcnt lgkmcnt(4)
	v_mfma_f32_16x16x32_bf16 v[140:143], v[80:83], v[156:159], v[140:143]
	v_mfma_f32_16x16x32_bf16 v[128:131], v[84:87], v[156:159], v[128:131]
	ds_read_b128 v[156:159], v168 offset:41216
	s_waitcnt lgkmcnt(4)
	v_mfma_f32_16x16x32_bf16 v[136:139], v[80:83], v[174:177], v[136:139]
	s_or_b32 s46, s9, 0x2000
	s_mov_b32 m0, s26
	s_nop 0
	buffer_load_dwordx4 v166, s[12:15], s46 offen lds
	v_mfma_f32_16x16x32_bf16 v[132:135], v[84:87], v[174:177], v[132:135]
	s_waitcnt lgkmcnt(3)
	v_mfma_f32_16x16x32_bf16 v[140:143], v[88:91], v[152:155], v[140:143]
	ds_read_b128 v[174:177], v168 offset:43008
	v_mfma_f32_16x16x32_bf16 v[128:131], v[92:95], v[152:155], v[128:131]
	ds_read_b128 v[152:155], v168 offset:43264
	s_waitcnt lgkmcnt(4)
	v_mfma_f32_16x16x32_bf16 v[136:139], v[88:91], v[144:147], v[136:139]
	v_mfma_f32_16x16x32_bf16 v[132:135], v[92:95], v[144:147], v[132:135]
	ds_read_b128 v[144:147], v168 offset:45056
	s_waitcnt lgkmcnt(4)
	v_mfma_f32_16x16x32_bf16 v[140:143], v[96:99], v[148:151], v[140:143]
	v_mfma_f32_16x16x32_bf16 v[128:131], v[100:103], v[148:151], v[128:131]
	ds_read_b128 v[148:151], v168 offset:45312
	s_waitcnt lgkmcnt(4)
	v_mfma_f32_16x16x32_bf16 v[136:139], v[96:99], v[156:159], v[136:139]
	s_or_b32 s46, s9, 0x8000
	s_mov_b32 m0, s27
	s_nop 0
	buffer_load_dwordx4 v166, s[12:15], s46 offen lds
	v_mfma_f32_16x16x32_bf16 v[132:135], v[100:103], v[156:159], v[132:135]
	s_waitcnt lgkmcnt(3)
	v_mfma_f32_16x16x32_bf16 v[140:143], v[104:107], v[174:177], v[140:143]
	ds_read_b128 v[178:181], v168 offset:47104
	v_mfma_f32_16x16x32_bf16 v[128:131], v[108:111], v[174:177], v[128:131]
	s_waitcnt lgkmcnt(3)
	v_mfma_f32_16x16x32_bf16 v[136:139], v[104:107], v[152:155], v[136:139]
	ds_read_b128 v[174:177], v168 offset:47360
	v_mfma_f32_16x16x32_bf16 v[132:135], v[108:111], v[152:155], v[132:135]
	ds_read_b128 v[156:159], v169
	s_waitcnt lgkmcnt(4)
	v_mfma_f32_16x16x32_bf16 v[140:143], v[112:115], v[144:147], v[140:143]
	v_mfma_f32_16x16x32_bf16 v[128:131], v[116:119], v[144:147], v[128:131]
	ds_read_b128 v[152:155], v170
	s_waitcnt lgkmcnt(4)
	v_mfma_f32_16x16x32_bf16 v[144:147], v[112:115], v[148:151], v[136:139]
	s_or_b32 s9, s9, 0xa000
	s_mov_b32 m0, s28
	s_nop 0
	buffer_load_dwordx4 v166, s[12:15], s9 offen lds
	v_mfma_f32_16x16x32_bf16 v[132:135], v[116:119], v[148:151], v[132:135]
	ds_read_b128 v[148:151], v171
	s_waitcnt lgkmcnt(4)
	v_mfma_f32_16x16x32_bf16 v[136:139], v[120:123], v[178:181], v[140:143]
	v_mfma_f32_16x16x32_bf16 v[128:131], v[124:127], v[178:181], v[128:131]
	s_waitcnt lgkmcnt(3)
	v_mfma_f32_16x16x32_bf16 v[140:143], v[120:123], v[174:177], v[144:147]
	s_nop 2
	ds_read_b128 v[144:147], v172
	v_mfma_f32_16x16x32_bf16 v[132:135], v[124:127], v[174:177], v[132:135]
	s_waitcnt vmcnt(4)
	s_barrier
	s_cmp_lg_u32 s8, s43
	s_cbranch_scc1 .LBB3_11
	s_and_saveexec_b64 s[8:9], s[0:1]
	s_cbranch_execnz .LBB3_38
	s_or_b64 exec, exec, s[8:9]
	s_and_saveexec_b64 s[8:9], s[2:3]
	s_cbranch_execnz .LBB3_39
